# RWKV and mLSTM wave-group barriers inside the chunk loops: LDS drain moved next to the arrive add so the lane-0 setup overlaps it; polling without s_sleep
# speedup vs baseline: 1.0141x; 1.0041x over previous
; #define LAS __attribute__((address_space(3)))
; __device__ __forceinline__ void rw_bar(LAS unsigned* cnt, unsigned& target, int lane) {
;     asm volatile("s_waitcnt lgkmcnt(0)" ::: "memory");
;     if (lane == 0) __hip_atomic_fetch_add(cnt, 1u, __ATOMIC_RELAXED, __HIP_MEMORY_SCOPE_WORKGROUP);
.LBB0_927:
	s_and_saveexec_b64 s[58:59], s[4:5]
	s_cbranch_execz .LBB0_930
	s_mov_b64 s[60:61], exec
	v_mbcnt_lo_u32_b32 v41, s60, 0
	v_mbcnt_hi_u32_b32 v41, s61, v41
	v_cmp_eq_u32_e32 vcc, 0, v41
	s_and_b64 s[62:63], exec, vcc
	s_mov_b64 exec, s[62:63]
	s_bcnt1_i32_b64 s0, s[60:61]
	v_mov_b32_e32 v41, s67
	v_mov_b32_e32 v67, s0
	s_waitcnt lgkmcnt(0)
	ds_add_u32 v41, v67

; __device__ __forceinline__ void rw_bar(LAS unsigned* cnt, unsigned& target, int lane) {
;     ...
;     target += 4u;
;     while ((unsigned)__builtin_amdgcn_readfirstlane((int)__hip_atomic_load(cnt, __ATOMIC_RELAXED, __HIP_MEMORY_SCOPE_WORKGROUP)) < target) __builtin_amdgcn_s_sleep(1);
.LBB0_932:
	v_mov_b32_e32 v41, s67
	ds_read_b32 v41, v41
	s_mov_b64 s[58:59], -1
	s_waitcnt lgkmcnt(0)
	v_readfirstlane_b32 s55, v41
	s_cmp_ge_u32 s55, s0
	s_cbranch_scc1 .LBB0_931
	s_mov_b64 s[58:59], 0
	s_branch .LBB0_931

; #define LAS __attribute__((address_space(3)))
; __device__ __forceinline__ unsigned long long pack4bf(f32x4 v) { return (unsigned long long)pk2(v[0], v[1]) | ((unsigned long long)pk2(v[2], v[3]) << 32); }
; __device__ __forceinline__ void rw_bar(LAS unsigned* cnt, unsigned& target, int lane) {
;     asm volatile("s_waitcnt lgkmcnt(0)" ::: "memory");
;     if (lane == 0) __hip_atomic_fetch_add(cnt, 1u, __ATOMIC_RELAXED, __HIP_MEMORY_SCOPE_WORKGROUP);
; __device__ __forceinline__ void mlstm_scan_unit(Frame& F, int unit, LAS unsigned* bcnt, unsigned& btarget) {
;     ...
;               *(LAS unsigned long long*)(Ls + t * 72 + 16 * jt + 4 * fq) = pack4bf(acc); } }
;         rw_bar(bcnt, btarget, lane);
.Lml_b_tail3:
	v_cvt_pk_bf16_f32 v148, v67, v148
	v_cvt_pk_bf16_f32 v149, v149, v150
	ds_write_b64 v110, v[148:149] offset:96
	s_and_saveexec_b64 s[58:59], s[4:5]
	s_xor_b64 s[58:59], exec, s[58:59]
	s_cbranch_execz .LBB0_944
	s_mov_b64 s[62:63], exec
	v_mbcnt_lo_u32_b32 v41, s62, 0
	v_mbcnt_hi_u32_b32 v41, s63, v41
	v_cmp_eq_u32_e32 vcc, 0, v41
	s_and_saveexec_b64 s[60:61], vcc
	s_bcnt1_i32_b64 s0, s[62:63]
	v_mov_b32_e32 v41, s67
	v_mov_b32_e32 v67, s0
	s_waitcnt lgkmcnt(0)
	ds_add_u32 v41, v67
	s_or_b64 exec, exec, s[60:61]

; #define LAS __attribute__((address_space(3)))
; __device__ __forceinline__ void mlstm_scan_unit(Frame& F, int unit, LAS unsigned* bcnt, unsigned& btarget) {
;     ...
;         { const int mi = w; f32x4 a1[3], a2[3];
; #pragma unroll
;           for (int n = 0; n < 3; ++n) { a1[n] = (f32x4){0.f, 0.f, 0.f, 0.f}; a2[n] = a1[n]; }
; #pragma unroll
;           for (int ks = 0; ks < 2; ++ks) { const s16x8 A = *(const LAS s16x8*)(Ls + (16 * mi + fr) * 72 + 32 * ks + 8 * fq);
; #pragma unroll
;               for (int n = 0; n < 3; ++n) a1[n] = __builtin_amdgcn_mfma_f32_16x16x32_bf16(A, tr_frag(Lv, VS, 32 * ks + 8 * fq, 16 * n, fr), a1[n], 0, 0, 0); }
; #pragma unroll
;           for (int ks = 0; ks < 4; ++ks) { const s16x8 A = *(const LAS s16x8*)(Lq + (16 * mi + fr) * 136 + 32 * ks + 8 * fq);
; #pragma unroll
;               for (int n = 0; n < 3; ++n) a2[n] = __builtin_amdgcn_mfma_f32_16x16x32_bf16(A, *(const LAS s16x8*)(cTc + (16 * n + fr) * 136 + 32 * ks + 8 * fq), a2[n], 0, 0, 0); }
;           const f32x4 mx4 = *(const LAS f32x4*)(smx + 16 * mi + 4 * fq), b4 = *(const LAS f32x4*)(sb + 16 * mi + 4 * fq);
; #pragma unroll
;           for (int rg_ = 0; rg_ < 4; ++rg_) { const float wi = __expf(mstate - mx4[rg_]); float den = a1[2][rg_] + wi * a2[2][rg_]; den = __shfl(den, lane & 48);
;               const float mt = b4[rg_] + mx4[rg_]; const float inv = __builtin_amdgcn_rcpf(fmaxf(fabsf(den), __expf(-mt))); float* hp = HRAW + (tk0 + 16 * mi + 4 * fq + rg_) * RD + mh * 256 + sl * 32 + fr;
;               hp[0] = (a1[0][rg_] + wi * a2[0][rg_]) * inv; hp[16] = (a1[1][rg_] + wi * a2[1][rg_]) * inv; } }
.LBB0_948:
	v_add_f32_e32 v41, v127, v66
	v_sub_f32_e32 v41, v41, v93
	v_mul_f32_e32 v41, 0x3fb8aa3b, v41
	v_exp_f32_e32 v100, v41
	v_add_u32_e32 v41, v110, v109
	s_lshl_b32 s0, s71, 6
	s_bitcmp1_b32 s71, 0
	s_cselect_b32 s58, 0x3300, 0
	v_add_u32_e32 v40, s58, v117
	ds_read_b128 v[180:183], v41
	ds_read_b64_tr_b16 v[188:189], v121
	ds_read_b64_tr_b16 v[190:191], v121 offset:448
	ds_read_b64_tr_b16 v[192:193], v121 offset:32
	ds_read_b64_tr_b16 v[194:195], v121 offset:480
	ds_read_b64_tr_b16 v[196:197], v121 offset:64
	ds_read_b64_tr_b16 v[198:199], v121 offset:512
	ds_read_b128 v[184:187], v41 offset:64
	ds_read_b64_tr_b16 v[200:201], v121 offset:3584
	ds_read_b64_tr_b16 v[202:203], v121 offset:4032
	ds_read_b64_tr_b16 v[204:205], v121 offset:3616
	ds_read_b64_tr_b16 v[206:207], v121 offset:4064
	ds_read_b64_tr_b16 v[208:209], v121 offset:3648
	ds_read_b64_tr_b16 v[210:211], v121 offset:4096
	ds_read_b128 v[212:215], v40
	ds_read_b128 v[228:231], v40 offset:4352
	ds_read_b128 v[216:219], v40 offset:64
	ds_read_b128 v[232:235], v40 offset:4416
	ds_read_b128 v[220:223], v40 offset:128
	ds_read_b128 v[152:155], v40 offset:4480
	ds_read_b128 v[224:227], v40 offset:192
	ds_read_b128 v[156:159], v40 offset:4544
	ds_read_b128 v[140:143], v111
	ds_read_b128 v[144:147], v112
	v_lshl_add_u64 v[148:149], v[98:99], 0, s[0:1]
	v_lshlrev_b64 v[148:149], 12, v[148:149]
	v_lshl_add_u64 v[150:151], v[96:97], 0, v[148:149]
	v_pk_mul_f32 v[56:57], v[56:57], v[100:101] op_sel_hi:[1,0]
	v_pk_mul_f32 v[54:55], v[54:55], v[100:101] op_sel_hi:[1,0]
	v_pk_mul_f32 v[60:61], v[60:61], v[100:101] op_sel_hi:[1,0]
	v_pk_mul_f32 v[58:59], v[58:59], v[100:101] op_sel_hi:[1,0]
	v_mul_f32_e64 v64, v64, v100
	v_mul_f32_e64 v65, v65, v100
	v_pk_mul_f32 v[62:63], v[62:63], v[100:101] op_sel_hi:[1,0]
	v_pk_mul_f32 v[44:45], v[44:45], v[100:101] op_sel_hi:[1,0]
	v_pk_mul_f32 v[42:43], v[42:43], v[100:101] op_sel_hi:[1,0]
	v_pk_mul_f32 v[48:49], v[48:49], v[100:101] op_sel_hi:[1,0]
	v_pk_mul_f32 v[46:47], v[46:47], v[100:101] op_sel_hi:[1,0]
	v_pk_mul_f32 v[52:53], v[52:53], v[100:101] op_sel_hi:[1,0]
	v_pk_mul_f32 v[50:51], v[50:51], v[100:101] op_sel_hi:[1,0]
	s_bitcmp1_b32 s70, 0
	s_cselect_b32 s55, 0x3300, 0
	s_waitcnt lgkmcnt(14)
	v_mfma_f32_16x16x32_bf16 v[66:69], v[180:183], v[188:191], 0
	v_mfma_f32_16x16x32_bf16 v[70:73], v[180:183], v[192:195], 0
	v_mfma_f32_16x16x32_bf16 v[74:77], v[180:183], v[196:199], 0
	v_mfma_f32_16x16x32_bf16 v[66:69], v[184:187], v[200:203], v[66:69]
	s_waitcnt lgkmcnt(12)
	v_mfma_f32_16x16x32_bf16 v[70:73], v[184:187], v[204:207], v[70:73]
	s_waitcnt lgkmcnt(10)
	v_mfma_f32_16x16x32_bf16 v[74:77], v[184:187], v[208:211], v[74:77]
	ds_read_b128 v[180:183], v40 offset:8704
	ds_read_b128 v[184:187], v40 offset:8768
	ds_read_b128 v[188:191], v40 offset:8832
	ds_read_b128 v[192:195], v40 offset:8896
	s_waitcnt lgkmcnt(12)
	v_mfma_f32_16x16x32_bf16 v[132:135], v[164:167], v[212:215], 0
	v_mfma_f32_16x16x32_bf16 v[136:139], v[164:167], v[228:231], 0
	s_waitcnt lgkmcnt(10)
	v_mfma_f32_16x16x32_bf16 v[132:135], v[168:171], v[216:219], v[132:135]
	v_mfma_f32_16x16x32_bf16 v[136:139], v[168:171], v[232:235], v[136:139]
	s_waitcnt lgkmcnt(8)
	v_mfma_f32_16x16x32_bf16 v[132:135], v[172:175], v[220:223], v[132:135]
	v_mfma_f32_16x16x32_bf16 v[136:139], v[172:175], v[152:155], v[136:139]
	s_waitcnt lgkmcnt(6)
	v_mfma_f32_16x16x32_bf16 v[132:135], v[176:179], v[224:227], v[132:135]
	v_mfma_f32_16x16x32_bf16 v[136:139], v[176:179], v[156:159], v[136:139]
	s_waitcnt lgkmcnt(3)
	v_mfma_f32_16x16x32_bf16 v[128:131], v[164:167], v[180:183], 0
	s_waitcnt lgkmcnt(2)
	v_mfma_f32_16x16x32_bf16 v[128:131], v[168:171], v[184:187], v[128:131]
	s_waitcnt lgkmcnt(1)
	v_mfma_f32_16x16x32_bf16 v[128:131], v[172:175], v[188:191], v[128:131]
	s_waitcnt lgkmcnt(0)
	v_mfma_f32_16x16x32_bf16 v[128:131], v[176:179], v[192:195], v[128:131]
	s_nop 2
	v_sub_f32_e32 v41, v127, v140
	v_mul_f32_e32 v41, 0x3fb8aa3b, v41
	v_exp_f32_e32 v41, v41
	s_nop 1
	v_fma_f32 v74, v128, v41, v74
	ds_bpermute_b32 v74, v126, v74
	ds_read_b64_tr_b16 v[196:197], v122 offset:62464
	ds_read_b64_tr_b16 v[198:199], v122 offset:63552
	ds_read_b64_tr_b16 v[212:213], v123
	ds_read_b64_tr_b16 v[214:215], v123 offset:448
	ds_read_b64_tr_b16 v[216:217], v123 offset:32
	v_add_f32_e32 v128, v140, v144
	v_mul_f32_e32 v128, 0xbfb8aa3b, v128
	v_exp_f32_e32 v128, v128
	v_fma_f32 v66, v132, v41, v66
	s_waitcnt lgkmcnt(5)
; #define LAS __attribute__((address_space(3)))
; __device__ __forceinline__ unsigned long long pack4bf(f32x4 v) { return (unsigned long long)pk2(v[0], v[1]) | ((unsigned long long)pk2(v[2], v[3]) << 32); }
; __device__ __forceinline__ void rw_bar(LAS unsigned* cnt, unsigned& target, int lane) {
;     asm volatile("s_waitcnt lgkmcnt(0)" ::: "memory");
;     if (lane == 0) __hip_atomic_fetch_add(cnt, 1u, __ATOMIC_RELAXED, __HIP_MEMORY_SCOPE_WORKGROUP);
; __device__ __forceinline__ void mlstm_scan_unit(Frame& F, int unit, LAS unsigned* bcnt, unsigned& btarget) {
;     ...
;           for (int rg_ = 0; rg_ < 4; ++rg_) { const float wi = __expf(mstate - mx4[rg_]); float den = a1[2][rg_] + wi * a2[2][rg_]; den = __shfl(den, lane & 48);
;               const float mt = b4[rg_] + mx4[rg_]; const float inv = __builtin_amdgcn_rcpf(fmaxf(fabsf(den), __expf(-mt))); float* hp = HRAW + (tk0 + 16 * mi + 4 * fq + rg_) * RD + mh * 256 + sl * 32 + fr;
;               hp[0] = (a1[0][rg_] + wi * a2[0][rg_]) * inv; hp[16] = (a1[1][rg_] + wi * a2[1][rg_]) * inv; } }
;         {
; #pragma unroll
;           for (int a = 0; a < 2; ++a) {
; #pragma unroll
;               for (int n = 0; n < 3; ++n) st[a][n] = st[a][n] * dec;
; #pragma unroll
;               for (int ks = 0; ks < 2; ++ks) { const s16x8 A = tr_frag(Lk, 136, 32 * ks + 8 * fq, 16 * (2 * w + a), fr);
; #pragma unroll
;                   for (int n = 0; n < 3; ++n) st[a][n] = __builtin_amdgcn_mfma_f32_16x16x32_bf16(A, tr_frag(Lvs, VS, 32 * ks + 8 * fq, 16 * n, fr), st[a][n], 0, 0, 0); }
; #pragma unroll
;               for (int n = 0; n < 3; ++n) *(LAS unsigned long long*)(cTn + (16 * n + fr) * 136 + 16 * (2 * w + a) + 4 * fq) = pack4bf(st[a][n]); } }
	v_max_f32_e64 v74, |v74|, |v74|
	v_fma_f32 v41, v136, v41, v70
	v_max_f32_e32 v74, v74, v128
	v_rcp_f32_e32 v74, v74
	v_add_f32_e32 v70, v141, v145
	v_mul_f32_e32 v70, 0xbfb8aa3b, v70
	v_exp_f32_e32 v70, v70
	v_mul_f32_e32 v41, v41, v74
	global_store_dword v[150:151], v41, off offset:64
	v_sub_f32_e32 v41, v127, v141
	v_mul_f32_e32 v41, 0x3fb8aa3b, v41
	v_exp_f32_e32 v41, v41
	v_mul_f32_e32 v66, v66, v74
	global_store_dword v[150:151], v66, off
	v_or_b32_e32 v74, 0x1000, v148
	v_fma_f32 v66, v129, v41, v75
	ds_bpermute_b32 v66, v126, v66
	ds_read_b64_tr_b16 v[218:219], v123 offset:480
	ds_read_b64_tr_b16 v[220:221], v123 offset:64
	ds_read_b64_tr_b16 v[222:223], v123 offset:512
	ds_read_b64_tr_b16 v[204:205], v122 offset:62496
	ds_read_b64_tr_b16 v[206:207], v122 offset:63584
	v_mov_b32_e32 v75, v149
	v_fma_f32 v67, v133, v41, v67
	v_fma_f32 v41, v137, v41, v71
	v_lshl_add_u64 v[74:75], v[96:97], 0, v[74:75]
	s_waitcnt lgkmcnt(5)
	v_max_f32_e64 v66, |v66|, |v66|
	v_max_f32_e32 v66, v66, v70
	v_rcp_f32_e32 v66, v66
	s_nop 0
	v_mul_f32_e32 v41, v41, v66
	global_store_dword v[74:75], v41, off offset:64
	v_sub_f32_e32 v41, v127, v142
	v_mul_f32_e32 v41, 0x3fb8aa3b, v41
	v_exp_f32_e32 v41, v41
	v_mul_f32_e32 v67, v67, v66
	global_store_dword v[74:75], v67, off
	v_add_f32_e32 v67, v142, v146
	v_fma_f32 v66, v130, v41, v76
	ds_bpermute_b32 v66, v126, v66
	ds_read_b64_tr_b16 v[200:201], v124 offset:62464
	ds_read_b64_tr_b16 v[202:203], v124 offset:63552
	ds_read_b64_tr_b16 v[224:225], v123 offset:3584
	ds_read_b64_tr_b16 v[226:227], v123 offset:4032
	ds_read_b64_tr_b16 v[228:229], v123 offset:3616
	v_mul_f32_e32 v67, 0xbfb8aa3b, v67
	v_exp_f32_e32 v67, v67
	v_fma_f32 v68, v134, v41, v68
	v_fma_f32 v41, v138, v41, v72
	s_waitcnt lgkmcnt(5)
	v_max_f32_e64 v66, |v66|, |v66|
	v_max_f32_e32 v66, v66, v67
	v_rcp_f32_e32 v70, v66
	v_or_b32_e32 v66, 0x2000, v148
	v_mov_b32_e32 v67, v149
	v_lshl_add_u64 v[66:67], v[96:97], 0, v[66:67]
	v_mul_f32_e32 v41, v41, v70
	global_store_dword v[66:67], v41, off offset:64
	v_sub_f32_e32 v41, v127, v143
	v_mul_f32_e32 v41, 0x3fb8aa3b, v41
	v_exp_f32_e32 v41, v41
	v_mul_f32_e32 v68, v68, v70
	global_store_dword v[66:67], v68, off
	v_add_f32_e32 v67, v143, v147
	v_fmac_f32_e32 v77, v131, v41
	ds_bpermute_b32 v66, v126, v77
	ds_read_b64_tr_b16 v[230:231], v123 offset:4064
	ds_read_b64_tr_b16 v[232:233], v123 offset:3648
	ds_read_b64_tr_b16 v[234:235], v123 offset:4096
	ds_read_b64_tr_b16 v[208:209], v124 offset:62496
	ds_read_b64_tr_b16 v[210:211], v124 offset:63584
	v_mul_f32_e32 v67, 0xbfb8aa3b, v67
	v_exp_f32_e32 v67, v67
	v_or_b32_e32 v148, 0x3000, v148
	v_fmac_f32_e32 v69, v135, v41
	s_waitcnt lgkmcnt(5)
	v_max_f32_e64 v66, |v66|, |v66|
	v_max_f32_e32 v66, v66, v67
	v_rcp_f32_e32 v68, v66
	v_fmac_f32_e32 v73, v139, v41
	v_lshl_add_u64 v[66:67], v[96:97], 0, v[148:149]
	v_mul_f32_e32 v69, v69, v68
	v_mul_f32_e32 v41, v73, v68
	global_store_dword v[66:67], v69, off
	global_store_dword v[66:67], v41, off offset:64
	v_add_u32_e32 v41, s55, v118
	s_waitcnt lgkmcnt(0)
	v_mfma_f32_16x16x32_bf16 v[54:57], v[196:199], v[212:215], v[54:57]
	v_mfma_f32_16x16x32_bf16 v[58:61], v[196:199], v[216:219], v[58:61]
	v_mfma_f32_16x16x32_bf16 v[62:65], v[196:199], v[220:223], v[62:65]
	v_mfma_f32_16x16x32_bf16 v[42:45], v[204:207], v[212:215], v[42:45]
	v_mfma_f32_16x16x32_bf16 v[46:49], v[204:207], v[216:219], v[46:49]
	v_mfma_f32_16x16x32_bf16 v[50:53], v[204:207], v[220:223], v[50:53]
	v_mfma_f32_16x16x32_bf16 v[54:57], v[200:203], v[224:227], v[54:57]
	v_mfma_f32_16x16x32_bf16 v[58:61], v[200:203], v[228:231], v[58:61]
	v_mfma_f32_16x16x32_bf16 v[62:65], v[200:203], v[232:235], v[62:65]
	v_mfma_f32_16x16x32_bf16 v[42:45], v[208:211], v[224:227], v[42:45]
	v_mfma_f32_16x16x32_bf16 v[46:49], v[208:211], v[228:231], v[46:49]
	v_mfma_f32_16x16x32_bf16 v[50:53], v[208:211], v[232:235], v[50:53]
	s_nop 2
	v_cvt_pk_bf16_f32 v66, v54, v55
	v_cvt_pk_bf16_f32 v67, v56, v57
	ds_write_b64 v41, v[66:67]
	v_cvt_pk_bf16_f32 v68, v58, v59
	v_cvt_pk_bf16_f32 v69, v60, v61
	ds_write_b64 v41, v[68:69] offset:4352
	v_cvt_pk_bf16_f32 v70, v62, v63
	v_cvt_pk_bf16_f32 v71, v64, v65
	ds_write_b64 v41, v[70:71] offset:8704
	v_cvt_pk_bf16_f32 v72, v42, v43
	v_cvt_pk_bf16_f32 v73, v44, v45
	ds_write_b64 v41, v[72:73] offset:32
	v_cvt_pk_bf16_f32 v74, v46, v47
	v_cvt_pk_bf16_f32 v75, v48, v49
	ds_write_b64 v41, v[74:75] offset:4384
	v_cvt_pk_bf16_f32 v76, v50, v51
	v_cvt_pk_bf16_f32 v77, v52, v53
	ds_write_b64 v41, v[76:77] offset:8736
	s_and_saveexec_b64 s[58:59], s[4:5]
	s_cbranch_execz .LBB0_951
	s_mov_b64 s[60:61], exec
	v_mbcnt_lo_u32_b32 v41, s60, 0
	v_mbcnt_hi_u32_b32 v41, s61, v41
	v_cmp_eq_u32_e32 vcc, 0, v41
	s_and_b64 s[62:63], exec, vcc
	s_mov_b64 exec, s[62:63]
	s_bcnt1_i32_b64 s0, s[60:61]
	v_mov_b32_e32 v41, s67
	v_mov_b32_e32 v66, s0
	s_waitcnt lgkmcnt(0)
	ds_add_u32 v41, v66

; __device__ __forceinline__ void rw_bar(LAS unsigned* cnt, unsigned& target, int lane) {
;     ...
;     target += 4u;
;     while ((unsigned)__builtin_amdgcn_readfirstlane((int)__hip_atomic_load(cnt, __ATOMIC_RELAXED, __HIP_MEMORY_SCOPE_WORKGROUP)) < target) __builtin_amdgcn_s_sleep(1);
.LBB0_953:
	v_mov_b32_e32 v41, s67
	ds_read_b32 v41, v41
	s_mov_b64 s[58:59], -1
	s_waitcnt lgkmcnt(0)
	v_readfirstlane_b32 s0, v41
	s_cmp_ge_u32 s0, s53
	s_cbranch_scc1 .LBB0_952
	s_mov_b64 s[58:59], 0
	s_branch .LBB0_952

; #define LAS __attribute__((address_space(3)))
; __device__ __forceinline__ void rw_bar(LAS unsigned* cnt, unsigned& target, int lane) {
;     asm volatile("s_waitcnt lgkmcnt(0)" ::: "memory");
;     if (lane == 0) __hip_atomic_fetch_add(cnt, 1u, __ATOMIC_RELAXED, __HIP_MEMORY_SCOPE_WORKGROUP);
.LBB0_996:
	s_and_saveexec_b64 s[4:5], s[6:7]
	s_cbranch_execz .LBB0_999
	s_mov_b64 s[96:97], exec
	v_mbcnt_lo_u32_b32 v2, s96, 0
	v_mbcnt_hi_u32_b32 v2, s97, v2
	v_cmp_eq_u32_e32 vcc, 0, v2
	s_and_b64 s[10:11], exec, vcc
	s_mov_b64 exec, s[10:11]
	s_bcnt1_i32_b64 s10, s[96:97]
	v_mov_b32_e32 v2, s12
	v_mov_b32_e32 v3, s10
	s_waitcnt lgkmcnt(0)
	ds_add_u32 v2, v3

; #define LAS __attribute__((address_space(3)))
; __device__ __forceinline__ float allreduce16(float x) { x += dppf<0x128>(x); x += dppf<0x124>(x); x += dppf<0x4E>(x); x += dppf<0xB1>(x); return x; }
; __device__ __forceinline__ unsigned long long pack4bf(f32x4 v) { return (unsigned long long)pk2(v[0], v[1]) | ((unsigned long long)pk2(v[2], v[3]) << 32); }
; __device__ __forceinline__ void rwkv_chunk_unit(Frame& F, int unit, LAS unsigned char* regB, LAS unsigned* bcnt, unsigned& btarget) {
;     ...
;             const f32x4 kkr = k1 * kkc; const float nrm = __builtin_amdgcn_rsqf(fmaxf(allreduce16((kkr[0] * kkr[0] + kkr[1] * kkr[1]) + (kkr[2] * kkr[2] + kkr[3] * kkr[3])), 1e-24f));
;             kkn[p_] = kkr * nrm; kmod[p_] = k1 * (1.f + (al[p_] - 1.f) * kac);
;             { const f32x4 rk_ = rr[p_] * kmod[p_] * rkc; const float dot = allreduce16((rk_[0] + rk_[1]) + (rk_[2] + rk_[3]));
;               if ((cs >> 3) == half) *(unsigned long long*)(BON + ((size_t)b * SEQ + ch * 32 + ts + 16 * p_) * RD + c0) = pack4bf(vv[p_] * dot); }
;             }
;         { const int tq = lane & 31, hq = lane >> 5; f32x4 c0v, c1v;
; #pragma unroll
;           for (int j = 0; j < 4; ++j) { c0v[j] = scan32(ws0[j]); c1v[j] = scan32(ws1[j]); }
;           *(LAS f32x4*)(csf + tq * 64 + 16 * w + 8 * hq) = c0v; *(LAS f32x4*)(csf + tq * 64 + 16 * w + 8 * hq + 4) = c1v; }
;         if (ch + 1 < SEQ / 32) RC_LOAD(ch + 1);
;         rw_bar(bcnt, btarget, lane);
; #pragma unroll
;         for (int p_ = 0; p_ < 2; ++p_) { const int t = ts + 16 * p_; const f32x4 cg = *(const LAS f32x4*)(csf + t * 64 + 4 * cs); f32x4 cgp = (f32x4){0.f, 0.f, 0.f, 0.f}; if (t > 0) cgp = *(const LAS f32x4*)(csf + (t - 1) * 64 + 4 * cs); f32x4 g, gp, gi;
; #pragma unroll
;           for (int j = 0; j < 4; ++j) { g[j] = __expf(cg[j]); gp[j] = __expf(cgp[j]); gi[j] = __expf(-cg[j]); }
;           *(LAS unsigned long long*)(At + t * KS + 4 * cs) = pack4bf(-(kkn[p_] * gp)); *(LAS unsigned long long*)(Bt + t * KS + 4 * cs) = pack4bf(kkn[p_] * al[p_] * gi);
;           *(LAS unsigned long long*)(Kt + t * KS + 4 * cs) = pack4bf(kmod[p_] * gi); *(LAS unsigned long long*)(Rt + t * KS + 4 * cs) = pack4bf(rr[p_] * g);
;           if ((cs >> 3) == half) *(LAS unsigned long long*)(Vv + t * LS + 4 * (cs & 7)) = pack4bf(vv[p_]);
;           if (t == 31) *(LAS f32x4*)(glf + 4 * cs) = g; }
;         rw_bar(bcnt, btarget, lane);
.LBB0_1001:
	v_mov_b32_e32 v2, s12
	ds_read_b32 v2, v2
	s_waitcnt lgkmcnt(0)
	v_readfirstlane_b32 s4, v2
	s_cmp_ge_u32 s4, s10
	s_mov_b64 s[4:5], -1
	s_cbranch_scc1 .LBB0_1000
	s_mov_b64 s[4:5], 0
	s_branch .LBB0_1000
.LBB0_1003:
	ds_read_b128 v[4:7], v180
	v_mov_b32_e32 v8, 0
	v_mov_b32_e32 v9, 0
	v_mov_b32_e32 v10, 0
	v_mov_b32_e32 v11, 0
	s_and_saveexec_b64 s[4:5], s[36:37]
	ds_read_b128 v[8:11], v181
	s_or_b64 exec, exec, s[4:5]
	v_add_f32_e32 v2, v200, v201
	v_max_f32_e32 v2, 0x179abe15, v2
	v_rsq_f32_e32 v200, v2
	s_waitcnt lgkmcnt(0)
	v_mul_f32_e32 v3, 0x3fb8aa3b, v8
	v_mul_f32_e32 v2, 0x3fb8aa3b, v4
	v_exp_f32_e32 v2, v2
	v_pk_mul_f32 v[44:45], v[44:45], v[200:201] op_sel_hi:[1,0]
	v_pk_mul_f32 v[46:47], v[46:47], v[200:201] op_sel_hi:[1,0]
	v_exp_f32_e32 v200, v3
	v_mul_f32_e32 v3, 0xbfb8aa3b, v4
	v_mul_f32_e32 v4, 0x3fb8aa3b, v9
	v_exp_f32_e32 v8, v3
	v_mul_f32_e32 v3, 0x3fb8aa3b, v5
	v_exp_f32_e32 v201, v4
	v_mul_f32_e32 v4, 0xbfb8aa3b, v5
	v_mul_f32_e32 v5, 0x3fb8aa3b, v10
	v_exp_f32_e32 v204, v5
	v_mul_f32_e32 v5, 0xbfb8aa3b, v6
	v_mul_f32_e32 v10, 0x3fb8aa3b, v11
	v_exp_f32_e32 v9, v4
	v_mul_f32_e32 v4, 0x3fb8aa3b, v6
	v_exp_f32_e32 v6, v5
	v_mul_f32_e32 v5, 0x3fb8aa3b, v7
	v_exp_f32_e32 v205, v10
	v_mul_f32_e32 v7, 0xbfb8aa3b, v7
	v_exp_f32_e32 v7, v7
	v_exp_f32_e32 v3, v3
	v_exp_f32_e32 v4, v4
	v_exp_f32_e32 v5, v5
	v_xor_b32_e32 v11, 0x80000000, v201
	v_xor_b32_e32 v10, 0x80000000, v200
	v_xor_b32_e32 v201, 0x80000000, v205
	v_xor_b32_e32 v200, 0x80000000, v204
	v_pk_mul_f32 v[18:19], v[44:45], v[18:19]
	v_pk_mul_f32 v[16:17], v[46:47], v[16:17]
	v_pk_mul_f32 v[200:201], v[44:45], v[200:201]
	v_pk_mul_f32 v[10:11], v[46:47], v[10:11]
	v_pk_mul_f32 v[18:19], v[18:19], v[6:7]
	v_pk_mul_f32 v[16:17], v[16:17], v[8:9]
	v_cvt_pk_bf16_f32 v10, v10, v11
	v_cvt_pk_bf16_f32 v11, v200, v201
	v_cvt_pk_bf16_f32 v16, v16, v17
	v_cvt_pk_bf16_f32 v17, v18, v19
	v_pk_mul_f32 v[6:7], v[36:37], v[6:7]
	v_pk_mul_f32 v[8:9], v[38:39], v[8:9]
	ds_write2st64_b64 v182, v[10:11], v[16:17] offset1:9
	v_cvt_pk_bf16_f32 v8, v8, v9
	v_cvt_pk_bf16_f32 v9, v6, v7
	v_pk_mul_f32 v[6:7], v[20:21], v[4:5]
	v_pk_mul_f32 v[10:11], v[22:23], v[2:3]
	s_nop 0
	v_cvt_pk_bf16_f32 v10, v10, v11
	v_cvt_pk_bf16_f32 v11, v6, v7
	ds_write2st64_b64 v182, v[8:9], v[10:11] offset0:18 offset1:27
	s_and_saveexec_b64 s[4:5], s[92:93]
	v_cvt_pk_bf16_f32 v6, v30, v31
	v_cvt_pk_bf16_f32 v7, v24, v25
	ds_write_b64 v194, v[6:7] offset:18432
	s_or_b64 exec, exec, s[4:5]
	s_mov_b64 s[4:5], exec
	v_readlane_b32 s10, v236, 31
	v_readlane_b32 s11, v236, 32
	s_and_b64 s[10:11], s[4:5], s[10:11]
	s_mov_b64 exec, s[10:11]
	ds_write_b128 v101, v[2:5]
	s_or_b64 exec, exec, s[4:5]
	v_add_f32_e32 v2, v202, v203
	v_max_f32_e32 v2, 0x179abe15, v2
	ds_read_b128 v[4:7], v183
	ds_read_b128 v[8:11], v184
	v_rsq_f32_e32 v2, v2
	s_nop 0
	v_pk_mul_f32 v[16:17], v[48:49], v[2:3] op_sel_hi:[1,0]
	v_pk_mul_f32 v[18:19], v[166:167], v[2:3] op_sel_hi:[1,0]
	s_waitcnt lgkmcnt(0)
	v_mul_f32_e32 v3, 0x3fb8aa3b, v8
	v_mul_f32_e32 v2, 0x3fb8aa3b, v4
	v_exp_f32_e32 v20, v3
	v_mul_f32_e32 v3, 0xbfb8aa3b, v4
	v_mul_f32_e32 v4, 0x3fb8aa3b, v9
	v_exp_f32_e32 v8, v3
	v_mul_f32_e32 v3, 0x3fb8aa3b, v5
	v_exp_f32_e32 v21, v4
	v_mul_f32_e32 v4, 0xbfb8aa3b, v5
	v_mul_f32_e32 v5, 0x3fb8aa3b, v10
	v_exp_f32_e32 v22, v5
	v_mul_f32_e32 v5, 0xbfb8aa3b, v6
	v_mul_f32_e32 v10, 0x3fb8aa3b, v11
	v_exp_f32_e32 v9, v4
	v_mul_f32_e32 v4, 0x3fb8aa3b, v6
	v_exp_f32_e32 v6, v5
	v_mul_f32_e32 v5, 0x3fb8aa3b, v7
	v_exp_f32_e32 v23, v10
	v_mul_f32_e32 v7, 0xbfb8aa3b, v7
	v_exp_f32_e32 v7, v7
	v_exp_f32_e32 v2, v2
	v_exp_f32_e32 v3, v3
	v_exp_f32_e32 v4, v4
	v_exp_f32_e32 v5, v5
	v_xor_b32_e32 v11, 0x80000000, v21
	v_xor_b32_e32 v10, 0x80000000, v20
	v_xor_b32_e32 v21, 0x80000000, v23
	v_xor_b32_e32 v20, 0x80000000, v22
	v_pk_mul_f32 v[14:15], v[16:17], v[14:15]
	v_pk_mul_f32 v[12:13], v[18:19], v[12:13]
	v_pk_mul_f32 v[20:21], v[16:17], v[20:21]
	v_pk_mul_f32 v[10:11], v[18:19], v[10:11]
	v_pk_mul_f32 v[14:15], v[14:15], v[6:7]
	v_pk_mul_f32 v[12:13], v[12:13], v[8:9]
	v_cvt_pk_bf16_f32 v10, v10, v11
	v_cvt_pk_bf16_f32 v11, v20, v21
	v_cvt_pk_bf16_f32 v12, v12, v13
	v_cvt_pk_bf16_f32 v13, v14, v15
	v_add_u32_e32 v14, 0x100, v182
	v_pk_mul_f32 v[6:7], v[40:41], v[6:7]
	v_pk_mul_f32 v[8:9], v[42:43], v[8:9]
	ds_write2st64_b64 v14, v[10:11], v[12:13] offset0:4 offset1:13
	v_cvt_pk_bf16_f32 v8, v8, v9
	v_cvt_pk_bf16_f32 v9, v6, v7
	v_pk_mul_f32 v[6:7], v[26:27], v[4:5]
	v_pk_mul_f32 v[10:11], v[28:29], v[2:3]
	s_nop 0
	v_cvt_pk_bf16_f32 v10, v10, v11
	v_cvt_pk_bf16_f32 v11, v6, v7
	ds_write2st64_b64 v14, v[8:9], v[10:11] offset0:22 offset1:31
	s_and_saveexec_b64 s[4:5], s[92:93]
	v_cvt_pk_bf16_f32 v6, v34, v35
	v_cvt_pk_bf16_f32 v7, v32, v33
	ds_write_b64 v194, v[6:7] offset:19712
	s_or_b64 exec, exec, s[4:5]
	s_mov_b64 s[4:5], exec
	v_readlane_b32 s10, v236, 33
	v_readlane_b32 s11, v236, 34
	s_and_b64 s[10:11], s[4:5], s[10:11]
	s_mov_b64 exec, s[10:11]
	ds_write_b128 v101, v[2:5]
	s_or_b64 exec, exec, s[4:5]
	s_and_saveexec_b64 s[4:5], s[6:7]
	s_xor_b64 s[4:5], exec, s[4:5]
	s_cbranch_execz .LBB0_1017
	s_mov_b64 s[10:11], exec
	v_mbcnt_lo_u32_b32 v2, s10, 0
	v_mbcnt_hi_u32_b32 v2, s11, v2
	v_cmp_eq_u32_e32 vcc, 0, v2
	s_and_saveexec_b64 s[96:97], vcc
	s_bcnt1_i32_b64 s10, s[10:11]
	v_mov_b32_e32 v2, s12
	v_mov_b32_e32 v3, s10
	s_waitcnt lgkmcnt(0)
	ds_add_u32 v2, v3
	s_or_b64 exec, exec, s[96:97]

; #define LAS __attribute__((address_space(3)))
; __device__ __forceinline__ unsigned long long pack4bf(f32x4 v) { return (unsigned long long)pk2(v[0], v[1]) | ((unsigned long long)pk2(v[2], v[3]) << 32); }
; __device__ __forceinline__ void rwkv_chunk_unit(Frame& F, int unit, LAS unsigned char* regB, LAS unsigned* bcnt, unsigned& btarget) {
;     ...
;           f32x4 tv; tv[0] = w == 0 ? Aq[0] : w == 1 ? Aq[4] : w == 2 ? Aq[8] : Aq[12]; tv[1] = w == 0 ? Aq[1] : w == 1 ? Aq[5] : w == 2 ? Aq[9] : Aq[13];
;           tv[2] = w == 0 ? Aq[2] : w == 1 ? Aq[6] : w == 2 ? Aq[10] : Aq[14]; tv[3] = w == 0 ? Aq[3] : w == 1 ? Aq[7] : w == 2 ? Aq[11] : Aq[15];
;           *(LAS unsigned long long*)(Acb + 32 * LS + tq * LS + 8 * w + 4 * hq) = pack4bf(tv); }
;         rw_bar(bcnt, btarget, lane);
; __device__ __forceinline__ void rw_bar(LAS unsigned* cnt, unsigned& target, int lane) {
;     asm volatile("s_waitcnt lgkmcnt(0)" ::: "memory");
;     if (lane == 0) __hip_atomic_fetch_add(cnt, 1u, __ATOMIC_RELAXED, __HIP_MEMORY_SCOPE_WORKGROUP);
.LBB0_1037:
	s_nop 3
	v_cvt_pk_bf16_f32 v2, v2, v3
	v_cvt_pk_bf16_f32 v3, v4, v5
	ds_write_b64 v189, v[2:3] offset:40960
	s_and_saveexec_b64 s[4:5], s[6:7]
	s_cbranch_execz .LBB0_1040
	s_mov_b64 s[10:11], exec
	v_mbcnt_lo_u32_b32 v2, s10, 0
	v_mbcnt_hi_u32_b32 v2, s11, v2
	v_cmp_eq_u32_e32 vcc, 0, v2
	s_and_b64 s[96:97], exec, vcc
	s_mov_b64 exec, s[96:97]
	s_bcnt1_i32_b64 s10, s[10:11]
	v_mov_b32_e32 v2, s12
	v_mov_b32_e32 v3, s10
	s_waitcnt lgkmcnt(0)
	ds_add_u32 v2, v3

; #define LAS __attribute__((address_space(3)))
; __device__ __forceinline__ unsigned long long pack4bf(f32x4 v) { return (unsigned long long)pk2(v[0], v[1]) | ((unsigned long long)pk2(v[2], v[3]) << 32); }
; __device__ __forceinline__ void rwkv_chunk_unit(Frame& F, int unit, LAS unsigned char* regB, LAS unsigned* bcnt, unsigned& btarget) {
;     ...
;         { f32x4 z = (f32x4){0.f, 0.f, 0.f, 0.f};
; #pragma unroll
;           for (int ks = 0; ks < 2; ++ks) { const s16x8 sb = *(const LAS s16x8*)(Sb + (16 * nj + fr) * KS + 32 * ks + 8 * fq);
;               z = __builtin_amdgcn_mfma_f32_16x16x32_bf16(*(const LAS s16x8*)(At + (16 * mi + fr) * KS + 32 * ks + 8 * fq), sb, z, 0, 0, 0);
;               yv = __builtin_amdgcn_mfma_f32_16x16x32_bf16(*(const LAS s16x8*)(Rt + (16 * mi + fr) * KS + 32 * ks + 8 * fq), sb, yv, 0, 0, 0); }
;           const s16x8 vt_ = tr_frag(Vv, LS, 8 * fq, 16 * nj, fr);
;           z = __builtin_amdgcn_mfma_f32_16x16x32_bf16(*(const LAS s16x8*)(G2b + (16 * mi + fr) * LS + 8 * fq), vt_, z, 0, 0, 0);
;           yv = __builtin_amdgcn_mfma_f32_16x16x32_bf16(*(const LAS s16x8*)(G4b + (16 * mi + fr) * LS + 8 * fq), vt_, yv, 0, 0, 0);
;           *(LAS unsigned long long*)(RHt + (16 * nj + fr) * LS + 16 * mi + 4 * fq) = pack4bf(z); }
;         rw_bar(bcnt, btarget, lane);
.LBB0_1044:
	ds_read_b128 v[2:5], v105 offset:20992
	ds_read_b128 v[6:9], v168
	ds_read_b128 v[10:13], v168 offset:13824
	s_waitcnt lgkmcnt(1)
	v_mfma_f32_16x16x32_bf16 v[6:9], v[6:9], v[2:5], 0
	s_waitcnt lgkmcnt(0)
	v_mfma_f32_16x16x32_bf16 v[2:5], v[10:13], v[2:5], 0
	ds_read_b128 v[10:13], v105 offset:21056
	ds_read_b128 v[14:17], v168 offset:64
	s_waitcnt lgkmcnt(0)
	v_mfma_f32_16x16x32_bf16 v[6:9], v[14:17], v[10:13], v[6:9]
	ds_read_b128 v[14:17], v168 offset:13888
	s_waitcnt lgkmcnt(0)
	v_mfma_f32_16x16x32_bf16 v[2:5], v[14:17], v[10:13], v[2:5]
	ds_read_b64_tr_b16 v[10:11], v172 offset:18432
	ds_read_b64_tr_b16 v[12:13], v172 offset:18752
	ds_read_b128 v[14:17], v173 offset:25600
	s_waitcnt lgkmcnt(0)
	v_mfma_f32_16x16x32_bf16 v[6:9], v[14:17], v[10:13], v[6:9]
	ds_read_b128 v[14:17], v173 offset:30720
	s_waitcnt lgkmcnt(0)
	v_mfma_f32_16x16x32_bf16 v[2:5], v[14:17], v[10:13], v[2:5]
	s_nop 4
	v_cvt_pk_bf16_f32 v6, v6, v7
	v_cvt_pk_bf16_f32 v7, v8, v9
	ds_write_b64 v174, v[6:7]
	s_and_saveexec_b64 s[4:5], s[6:7]
	s_cbranch_execz .LBB0_1047
	s_mov_b64 s[10:11], exec
	v_mbcnt_lo_u32_b32 v6, s10, 0
	v_mbcnt_hi_u32_b32 v6, s11, v6
	v_cmp_eq_u32_e32 vcc, 0, v6
	s_and_b64 s[96:97], exec, vcc
	s_mov_b64 exec, s[96:97]
	s_bcnt1_i32_b64 s10, s[10:11]
	v_mov_b32_e32 v6, s12
	v_mov_b32_e32 v7, s10
	s_waitcnt lgkmcnt(0)
	ds_add_u32 v6, v7

; #define LAS __attribute__((address_space(3)))
; __device__ __forceinline__ unsigned long long pack4bf(f32x4 v) { return (unsigned long long)pk2(v[0], v[1]) | ((unsigned long long)pk2(v[2], v[3]) << 32); }
; __device__ __forceinline__ void rwkv_chunk_unit(Frame& F, int unit, LAS unsigned char* regB, LAS unsigned* bcnt, unsigned& btarget) {
;     ...
;         { f32x4 z = (f32x4){0.f, 0.f, 0.f, 0.f};
;           z = __builtin_amdgcn_mfma_f32_16x16x32_bf16(*(const LAS s16x8*)(Acb + 32 * LS + (16 * mi + fr) * LS + 8 * fq), *(const LAS s16x8*)(RHt + (16 * nj + fr) * LS + 8 * fq), z, 0, 0, 0);
;           *(LAS unsigned long long*)(Ubt + (16 * nj + fr) * LS + 16 * mi + 4 * fq) = pack4bf(z); }
;         rw_bar(bcnt, btarget, lane);
; __device__ __forceinline__ void rw_bar(LAS unsigned* cnt, unsigned& target, int lane) {
;     ...
;     target += 4u;
;     while ((unsigned)__builtin_amdgcn_readfirstlane((int)__hip_atomic_load(cnt, __ATOMIC_RELAXED, __HIP_MEMORY_SCOPE_WORKGROUP)) < target) __builtin_amdgcn_s_sleep(1);
.LBB0_1049:
	v_mov_b32_e32 v6, s12
	ds_read_b32 v6, v6
	s_waitcnt lgkmcnt(0)
	v_readfirstlane_b32 s4, v6
	s_cmp_ge_u32 s4, s10
	s_mov_b64 s[4:5], -1
	s_cbranch_scc1 .LBB0_1048
	s_mov_b64 s[4:5], 0
	s_branch .LBB0_1048
.LBB0_1051:
	ds_read_b128 v[6:9], v173 offset:40960
	ds_read_b128 v[10:13], v175
	s_waitcnt lgkmcnt(0)
	v_mfma_f32_16x16x32_bf16 v[6:9], v[6:9], v[10:13], 0
	s_nop 7
	v_cvt_pk_bf16_f32 v6, v6, v7
	v_cvt_pk_bf16_f32 v7, v8, v9
	ds_write_b64 v176, v[6:7]
	s_and_saveexec_b64 s[4:5], s[6:7]
	s_cbranch_execz .LBB0_1054
	s_mov_b64 s[10:11], exec
	v_mbcnt_lo_u32_b32 v6, s10, 0
	v_mbcnt_hi_u32_b32 v6, s11, v6
	v_cmp_eq_u32_e32 vcc, 0, v6
	s_and_b64 s[96:97], exec, vcc
	s_mov_b64 exec, s[96:97]
	s_bcnt1_i32_b64 s10, s[10:11]
	v_mov_b32_e32 v6, s12
	v_mov_b32_e32 v7, s10
	s_waitcnt lgkmcnt(0)
	ds_add_u32 v6, v7

; __device__ __forceinline__ void rw_bar(LAS unsigned* cnt, unsigned& target, int lane) {
;     ...
;     target += 4u;
;     while ((unsigned)__builtin_amdgcn_readfirstlane((int)__hip_atomic_load(cnt, __ATOMIC_RELAXED, __HIP_MEMORY_SCOPE_WORKGROUP)) < target) __builtin_amdgcn_s_sleep(1);
.LBB0_1056:
	v_mov_b32_e32 v6, s12
	ds_read_b32 v6, v6
	s_waitcnt lgkmcnt(0)
	v_readfirstlane_b32 s4, v6
	s_cmp_ge_u32 s4, s13
	s_mov_b64 s[4:5], -1
	s_cbranch_scc1 .LBB0_1055
	s_mov_b64 s[4:5], 0
	s_branch .LBB0_1055
